# static priority raise (s_setprio 3) for the short MFMA GEMM blocks of K1 so they finish first; scan waves at default priority; otherwise the ring-16 hybrid
# speedup vs baseline: 1.0291x; 1.0291x over previous
_Z9k1_kernelPKfS0_S0_PDF16_PiPfP15HIP_vector_typeIiLj2EES6_:
	s_cmpk_lt_u32 s2, 0x60
	s_cbranch_scc0 .Lk1_scan
	s_setprio 3
	s_load_dwordx4 s[4:7], s[0:1], 0x8
	s_load_dwordx2 s[8:9], s[0:1], 0x18
	v_and_b32_e32 v1, 63, v0
	v_readfirstlane_b32 s3, v0
	v_lshrrev_b32_e32 v122, 3, v0
	v_and_b32_e32 v128, 7, v0
	v_lshlrev_b32_e32 v122, 10, v122
	v_lshl_or_b32 v122, v128, 4, v122
	v_lshrrev_b32_e32 v123, 5, v0
	v_and_b32_e32 v129, 31, v0
	v_lshlrev_b32_e32 v123, 9, v123
	v_lshl_or_b32 v123, v129, 4, v123
	v_lshrrev_b32_e32 v124, 3, v0
	v_mul_u32_u24_e32 v124, 0x90, v124
	v_lshl_add_u32 v132, v128, 3, v124
	v_add_u32_e32 v133, 0x1200, v132
	v_add_u32_e32 v134, 0x2400, v132
	v_add_u32_e32 v135, 0x3600, v132
	v_add_u32_e32 v125, 0x4800, v123
	v_and_b32_e32 v130, 31, v1
	v_lshrrev_b32_e32 v131, 5, v1
	s_lshr_b32 s3, s3, 6
	s_lshl_b32 s10, s3, 5
	v_add_u32_e32 v126, s10, v130
	v_mul_u32_u24_e32 v126, 0x90, v126
	v_lshl_add_u32 v126, v131, 6, v126
	v_lshlrev_b32_e32 v127, 9, v131
	v_lshl_add_u32 v127, v130, 4, v127
	v_add_u32_e32 v127, 0x4800, v127
	v_mov_b32_e32 v2, 0
	v_mov_b32_e32 v3, 0
	v_mov_b32_e32 v4, 0
	v_mov_b32_e32 v5, 0
	v_mov_b32_e32 v6, 0
	v_mov_b32_e32 v7, 0
	v_mov_b32_e32 v8, 0
	v_mov_b32_e32 v9, 0
	v_mov_b32_e32 v10, 0
	v_mov_b32_e32 v11, 0
	v_mov_b32_e32 v12, 0
	v_mov_b32_e32 v13, 0
	v_mov_b32_e32 v14, 0
	v_mov_b32_e32 v15, 0
	v_mov_b32_e32 v16, 0
	v_mov_b32_e32 v17, 0
	v_mov_b32_e32 v18, 0
	v_mov_b32_e32 v19, 0
	v_mov_b32_e32 v20, 0
	v_mov_b32_e32 v21, 0
	v_mov_b32_e32 v22, 0
	v_mov_b32_e32 v23, 0
	v_mov_b32_e32 v24, 0
	v_mov_b32_e32 v25, 0
	v_mov_b32_e32 v26, 0
	v_mov_b32_e32 v27, 0
	v_mov_b32_e32 v28, 0
	v_mov_b32_e32 v29, 0
	v_mov_b32_e32 v30, 0
	v_mov_b32_e32 v31, 0
	v_mov_b32_e32 v32, 0
	v_mov_b32_e32 v33, 0
	v_mov_b32_e32 v34, 0
	v_mov_b32_e32 v35, 0
	v_mov_b32_e32 v36, 0
	v_mov_b32_e32 v37, 0
	v_mov_b32_e32 v38, 0
	v_mov_b32_e32 v39, 0
	v_mov_b32_e32 v40, 0
	v_mov_b32_e32 v41, 0
	v_mov_b32_e32 v42, 0
	v_mov_b32_e32 v43, 0
	v_mov_b32_e32 v44, 0
	v_mov_b32_e32 v45, 0
	v_mov_b32_e32 v46, 0
	v_mov_b32_e32 v47, 0
	v_mov_b32_e32 v48, 0
	v_mov_b32_e32 v49, 0
	v_mov_b32_e32 v50, 0
	v_mov_b32_e32 v51, 0
	v_mov_b32_e32 v52, 0
	v_mov_b32_e32 v53, 0
	v_mov_b32_e32 v54, 0
	v_mov_b32_e32 v55, 0
	v_mov_b32_e32 v56, 0
	v_mov_b32_e32 v57, 0
	v_mov_b32_e32 v58, 0
	v_mov_b32_e32 v59, 0
	v_mov_b32_e32 v60, 0
	v_mov_b32_e32 v61, 0
	v_mov_b32_e32 v62, 0
	v_mov_b32_e32 v63, 0
	v_mov_b32_e32 v64, 0
	v_mov_b32_e32 v65, 0
	s_waitcnt lgkmcnt(0)
	s_lshl_b32 s11, s2, 17
	s_add_u32 s12, s4, s11
	s_addc_u32 s13, s5, 0
	s_add_u32 s14, s12, 0x8000
	s_addc_u32 s15, s13, 0
	s_add_u32 s16, s14, 0x8000
	s_addc_u32 s17, s15, 0
	s_add_u32 s18, s16, 0x8000
	s_addc_u32 s19, s17, 0
	s_add_u32 s20, s6, 0x1000
	s_addc_u32 s21, s7, 0
	s_add_u32 s22, s20, 0x1000
	s_addc_u32 s23, s21, 0
	s_add_u32 s24, s22, 0x1000
	s_addc_u32 s25, s23, 0
	global_load_dwordx4 v[90:93], v122, s[12:13]
	global_load_dwordx4 v[94:97], v122, s[14:15]
	global_load_dwordx4 v[98:101], v122, s[16:17]
	global_load_dwordx4 v[102:105], v122, s[18:19]
	global_load_dwordx4 v[106:109], v123, s[6:7]
	global_load_dwordx4 v[110:113], v123, s[20:21]
	global_load_dwordx4 v[114:117], v123, s[22:23]
	global_load_dwordx4 v[118:121], v123, s[24:25]
	s_mov_b32 s26, 0
